# GEMM tile start (in-proj, out, gate/up, down): accumulator zero fill (62 moves per wave per tile) removed, peeled first K trip takes inline-zero C
# speedup vs baseline: 1.0013x; 1.0013x over previous
.LBB0_212:
	s_add_u32 s12, s12, 0x40080
	s_addc_u32 s13, s13, 0
	s_add_u32 s7, s14, 0x100
	s_addc_u32 s28, s15, 0
	s_mov_b32 s29, -2
	s_add_u32 s14, s12, 0xfffc0080
	s_addc_u32 s15, s13, -1
	s_add_i32 s36, 0, 0x10000
	s_cmp_eq_u32 s29, 12
	s_cselect_b32 s17, s9, s15
	s_cselect_b32 s16, s8, s14
	s_cselect_b32 s15, s11, s28
	s_cselect_b32 s14, s10, s7
	s_add_i32 s42, 0, 0x14000
	v_add_u32_e32 v158, s36, v147
	v_add_u32_e32 v174, s42, v147
	ds_read_b128 v[142:145], v158
	ds_read_b128 v[150:153], v158 offset:1024
	ds_read_b128 v[154:157], v158 offset:2048
	ds_read_b128 v[158:161], v158 offset:3072
	ds_read_b128 v[162:165], v174
	ds_read_b128 v[166:169], v174 offset:1024
	ds_read_b128 v[170:173], v174 offset:2048
	ds_read_b128 v[174:177], v174 offset:3072
	v_lshl_add_u64 v[190:191], s[12:13], 0, v[138:139]
	s_add_i32 m0, s19, 0xc000
	ds_read_b128 v[178:181], v149
	ds_read_b128 v[182:185], v149 offset:1024
	ds_read_b128 v[186:189], v149 offset:2048
	ds_read_b128 v[198:201], v149 offset:3072
	ds_read_b128 v[202:205], v149 offset:4096
	ds_read_b128 v[206:209], v149 offset:5120
	ds_read_b128 v[210:213], v149 offset:6144
	ds_read_b128 v[214:217], v149 offset:7168
	global_load_lds_dwordx4 v[190:191], off
	v_lshl_add_u64 v[190:191], s[12:13], 0, v[140:141]
	s_add_i32 m0, s19, 0xe000
	s_nop 0
	global_load_lds_dwordx4 v[190:191], off
	s_waitcnt vmcnt(8)
	s_waitcnt lgkmcnt(0)
	s_barrier
	s_setprio 1
	s_waitcnt lgkmcnt(0)
	v_mfma_f32_16x16x32_bf16 v[126:129], v[142:145], v[178:181], 0
	v_mfma_f32_16x16x32_bf16 v[122:125], v[154:157], v[178:181], 0
	v_mfma_f32_16x16x32_bf16 v[110:113], v[142:145], v[186:189], 0
	v_mfma_f32_16x16x32_bf16 v[106:109], v[154:157], v[186:189], 0
	v_mfma_f32_16x16x32_bf16 v[94:97], v[142:145], v[202:205], 0
	v_mfma_f32_16x16x32_bf16 v[90:93], v[154:157], v[202:205], 0
	v_mfma_f32_16x16x32_bf16 v[78:81], v[142:145], v[210:213], 0
	v_mfma_f32_16x16x32_bf16 v[74:77], v[154:157], v[210:213], 0
	v_mfma_f32_16x16x32_bf16 v[126:129], v[150:153], v[182:185], v[126:129]
	v_mfma_f32_16x16x32_bf16 v[122:125], v[158:161], v[182:185], v[122:125]
	v_mfma_f32_16x16x32_bf16 v[110:113], v[150:153], v[198:201], v[110:113]
	v_mfma_f32_16x16x32_bf16 v[106:109], v[158:161], v[198:201], v[106:109]
	v_mfma_f32_16x16x32_bf16 v[94:97], v[150:153], v[206:209], v[94:97]
	v_mfma_f32_16x16x32_bf16 v[90:93], v[158:161], v[206:209], v[90:93]
	v_mfma_f32_16x16x32_bf16 v[78:81], v[150:153], v[214:217], v[78:81]
	v_mfma_f32_16x16x32_bf16 v[74:77], v[158:161], v[214:217], v[74:77]
	s_setprio 0
	s_setprio 1
	v_mfma_f32_16x16x32_bf16 v[118:121], v[162:165], v[178:181], 0
	v_mfma_f32_16x16x32_bf16 v[114:117], v[170:173], v[178:181], 0
	v_mfma_f32_16x16x32_bf16 v[102:105], v[162:165], v[186:189], 0
	v_mfma_f32_16x16x32_bf16 v[98:101], v[170:173], v[186:189], 0
	v_mfma_f32_16x16x32_bf16 v[86:89], v[162:165], v[202:205], 0
	v_mfma_f32_16x16x32_bf16 v[82:85], v[170:173], v[202:205], 0
	v_mfma_f32_16x16x32_bf16 v[70:73], v[162:165], v[210:213], 0
	v_mfma_f32_16x16x32_bf16 v[66:69], v[170:173], v[210:213], 0
	v_mfma_f32_16x16x32_bf16 v[118:121], v[166:169], v[182:185], v[118:121]
	v_mfma_f32_16x16x32_bf16 v[114:117], v[174:177], v[182:185], v[114:117]
	v_mfma_f32_16x16x32_bf16 v[102:105], v[166:169], v[198:201], v[102:105]
	v_mfma_f32_16x16x32_bf16 v[98:101], v[174:177], v[198:201], v[98:101]
	v_mfma_f32_16x16x32_bf16 v[86:89], v[166:169], v[206:209], v[86:89]
	v_mfma_f32_16x16x32_bf16 v[82:85], v[174:177], v[206:209], v[82:85]
	v_mfma_f32_16x16x32_bf16 v[70:73], v[166:169], v[214:217], v[70:73]
	v_mfma_f32_16x16x32_bf16 v[66:69], v[174:177], v[214:217], v[66:69]
	s_setprio 0
	s_barrier
	s_add_i32 s36, s36, s18
	v_lshl_add_u64 v[190:191], s[14:15], 0, v[130:131]
	s_mov_b32 m0, s36
	ds_read_b128 v[178:181], v149 offset:16384
	ds_read_b128 v[182:185], v149 offset:17408
	ds_read_b128 v[186:189], v149 offset:18432
	ds_read_b128 v[198:201], v149 offset:19456
	ds_read_b128 v[202:205], v149 offset:20480
	ds_read_b128 v[206:209], v149 offset:21504
	ds_read_b128 v[210:213], v149 offset:22528
	ds_read_b128 v[214:217], v149 offset:23552
	global_load_lds_dwordx4 v[190:191], off
	s_add_i32 m0, s36, 0x2000
	s_add_u32 s36, s14, 0x40000
	v_lshl_add_u64 v[218:219], s[14:15], 0, v[132:133]
	s_addc_u32 s37, s15, 0
	s_add_i32 s42, s42, s18
	global_load_lds_dwordx4 v[218:219], off
	v_lshl_add_u64 v[220:221], s[36:37], 0, v[130:131]
	s_mov_b32 m0, s42
	v_lshl_add_u64 v[222:223], s[16:17], 0, v[134:135]
	global_load_lds_dwordx4 v[220:221], off
	v_lshl_add_u64 v[220:221], s[36:37], 0, v[132:133]
	s_add_i32 m0, s42, 0x2000
	s_nop 0
	global_load_lds_dwordx4 v[220:221], off
	v_lshl_add_u64 v[220:221], s[16:17], 0, v[136:137]
	s_mov_b32 m0, s19
	s_nop 0
	global_load_lds_dwordx4 v[220:221], off
	s_mov_b32 m0, s20
	s_nop 0
	global_load_lds_dwordx4 v[222:223], off
	s_waitcnt vmcnt(8)
	s_waitcnt lgkmcnt(0)
	s_barrier
	s_setprio 1
	s_waitcnt lgkmcnt(0)
	v_mfma_f32_16x16x32_bf16 v[62:65], v[142:145], v[178:181], 0
	v_mfma_f32_16x16x32_bf16 v[58:61], v[154:157], v[178:181], 0
	v_mfma_f32_16x16x32_bf16 v[46:49], v[142:145], v[186:189], 0
	v_mfma_f32_16x16x32_bf16 v[42:45], v[154:157], v[186:189], 0
	v_mfma_f32_16x16x32_bf16 v[30:33], v[142:145], v[202:205], 0
	v_mfma_f32_16x16x32_bf16 v[26:29], v[154:157], v[202:205], 0
	v_mfma_f32_16x16x32_bf16 v[14:17], v[142:145], v[210:213], 0
	v_mfma_f32_16x16x32_bf16 v[10:13], v[154:157], v[210:213], 0
	v_mfma_f32_16x16x32_bf16 v[62:65], v[150:153], v[182:185], v[62:65]
	v_mfma_f32_16x16x32_bf16 v[58:61], v[158:161], v[182:185], v[58:61]
	v_mfma_f32_16x16x32_bf16 v[46:49], v[150:153], v[198:201], v[46:49]
	v_mfma_f32_16x16x32_bf16 v[42:45], v[158:161], v[198:201], v[42:45]
	v_mfma_f32_16x16x32_bf16 v[30:33], v[150:153], v[206:209], v[30:33]
	v_mfma_f32_16x16x32_bf16 v[26:29], v[158:161], v[206:209], v[26:29]
	v_mfma_f32_16x16x32_bf16 v[14:17], v[150:153], v[214:217], v[14:17]
	v_mfma_f32_16x16x32_bf16 v[10:13], v[158:161], v[214:217], v[10:13]
	s_setprio 0
	s_setprio 1
	v_mfma_f32_16x16x32_bf16 v[54:57], v[162:165], v[178:181], 0
	v_mfma_f32_16x16x32_bf16 v[50:53], v[170:173], v[178:181], 0
	v_mfma_f32_16x16x32_bf16 v[38:41], v[162:165], v[186:189], 0
	v_mfma_f32_16x16x32_bf16 v[34:37], v[170:173], v[186:189], 0
	v_mfma_f32_16x16x32_bf16 v[22:25], v[162:165], v[202:205], 0
	v_mfma_f32_16x16x32_bf16 v[18:21], v[170:173], v[202:205], 0
	v_mfma_f32_16x16x32_bf16 v[6:9], v[162:165], v[210:213], 0
	v_mfma_f32_16x16x32_bf16 v[2:5], v[170:173], v[210:213], 0
	v_mfma_f32_16x16x32_bf16 v[54:57], v[166:169], v[182:185], v[54:57]
	v_mfma_f32_16x16x32_bf16 v[50:53], v[174:177], v[182:185], v[50:53]
	v_mfma_f32_16x16x32_bf16 v[38:41], v[166:169], v[198:201], v[38:41]
	v_mfma_f32_16x16x32_bf16 v[34:37], v[174:177], v[198:201], v[34:37]
	v_mfma_f32_16x16x32_bf16 v[22:25], v[166:169], v[206:209], v[22:25]
	v_mfma_f32_16x16x32_bf16 v[18:21], v[174:177], v[206:209], v[18:21]
	v_mfma_f32_16x16x32_bf16 v[6:9], v[166:169], v[214:217], v[6:9]
	v_mfma_f32_16x16x32_bf16 v[2:5], v[174:177], v[214:217], v[2:5]
	s_setprio 0
	s_barrier
	s_add_i32 s36, 0, 0x18000
	s_add_i32 s37, 0, 0x1c000
	v_add_u32_e32 v158, s36, v147
	v_add_u32_e32 v174, s37, v147
	ds_read_b128 v[142:145], v158
	ds_read_b128 v[150:153], v158 offset:1024
	ds_read_b128 v[154:157], v158 offset:2048
	ds_read_b128 v[158:161], v158 offset:3072
	ds_read_b128 v[162:165], v174
	ds_read_b128 v[166:169], v174 offset:1024
	ds_read_b128 v[170:173], v174 offset:2048
	ds_read_b128 v[174:177], v174 offset:3072
	s_add_u32 s16, s16, 0x40000
	s_addc_u32 s17, s17, 0
	s_mov_b32 m0, s21
	v_lshl_add_u64 v[224:225], s[16:17], 0, v[136:137]
	ds_read_b128 v[178:181], v149 offset:32768
	ds_read_b128 v[182:185], v149 offset:33792
	ds_read_b128 v[186:189], v149 offset:34816
	ds_read_b128 v[198:201], v149 offset:35840
	ds_read_b128 v[202:205], v149 offset:36864
	ds_read_b128 v[206:209], v149 offset:37888
	ds_read_b128 v[210:213], v149 offset:38912
	ds_read_b128 v[214:217], v149 offset:39936
	global_load_lds_dwordx4 v[224:225], off
	v_lshl_add_u64 v[224:225], s[16:17], 0, v[134:135]
	s_mov_b32 m0, s22
	s_nop 0
	global_load_lds_dwordx4 v[224:225], off
	s_waitcnt vmcnt(8)
	s_waitcnt lgkmcnt(0)
	s_barrier
	s_setprio 1
	s_waitcnt lgkmcnt(0)
	v_mfma_f32_16x16x32_bf16 v[126:129], v[142:145], v[178:181], v[126:129]
	v_mfma_f32_16x16x32_bf16 v[122:125], v[154:157], v[178:181], v[122:125]
	v_mfma_f32_16x16x32_bf16 v[110:113], v[142:145], v[186:189], v[110:113]
	v_mfma_f32_16x16x32_bf16 v[106:109], v[154:157], v[186:189], v[106:109]
	v_mfma_f32_16x16x32_bf16 v[94:97], v[142:145], v[202:205], v[94:97]
	v_mfma_f32_16x16x32_bf16 v[90:93], v[154:157], v[202:205], v[90:93]
	v_mfma_f32_16x16x32_bf16 v[78:81], v[142:145], v[210:213], v[78:81]
	v_mfma_f32_16x16x32_bf16 v[74:77], v[154:157], v[210:213], v[74:77]
	v_mfma_f32_16x16x32_bf16 v[126:129], v[150:153], v[182:185], v[126:129]
	v_mfma_f32_16x16x32_bf16 v[122:125], v[158:161], v[182:185], v[122:125]
	v_mfma_f32_16x16x32_bf16 v[110:113], v[150:153], v[198:201], v[110:113]
	v_mfma_f32_16x16x32_bf16 v[106:109], v[158:161], v[198:201], v[106:109]
	v_mfma_f32_16x16x32_bf16 v[94:97], v[150:153], v[206:209], v[94:97]
	v_mfma_f32_16x16x32_bf16 v[90:93], v[158:161], v[206:209], v[90:93]
	v_mfma_f32_16x16x32_bf16 v[78:81], v[150:153], v[214:217], v[78:81]
	v_mfma_f32_16x16x32_bf16 v[74:77], v[158:161], v[214:217], v[74:77]
	s_setprio 0
	s_setprio 1
	v_mfma_f32_16x16x32_bf16 v[118:121], v[162:165], v[178:181], v[118:121]
	v_mfma_f32_16x16x32_bf16 v[114:117], v[170:173], v[178:181], v[114:117]
	v_mfma_f32_16x16x32_bf16 v[102:105], v[162:165], v[186:189], v[102:105]
	v_mfma_f32_16x16x32_bf16 v[98:101], v[170:173], v[186:189], v[98:101]
	v_mfma_f32_16x16x32_bf16 v[86:89], v[162:165], v[202:205], v[86:89]
	v_mfma_f32_16x16x32_bf16 v[82:85], v[170:173], v[202:205], v[82:85]
	v_mfma_f32_16x16x32_bf16 v[70:73], v[162:165], v[210:213], v[70:73]
	v_mfma_f32_16x16x32_bf16 v[66:69], v[170:173], v[210:213], v[66:69]
	v_mfma_f32_16x16x32_bf16 v[118:121], v[166:169], v[182:185], v[118:121]
	v_mfma_f32_16x16x32_bf16 v[114:117], v[174:177], v[182:185], v[114:117]
	v_mfma_f32_16x16x32_bf16 v[102:105], v[166:169], v[198:201], v[102:105]
	v_mfma_f32_16x16x32_bf16 v[98:101], v[174:177], v[198:201], v[98:101]
	v_mfma_f32_16x16x32_bf16 v[86:89], v[166:169], v[206:209], v[86:89]
	v_mfma_f32_16x16x32_bf16 v[82:85], v[174:177], v[206:209], v[82:85]
	v_mfma_f32_16x16x32_bf16 v[70:73], v[166:169], v[214:217], v[70:73]
	v_mfma_f32_16x16x32_bf16 v[66:69], v[174:177], v[214:217], v[66:69]
	s_setprio 0
	s_barrier
	s_add_i32 s16, s36, s18
	v_lshl_add_u64 v[190:191], v[190:191], 0, s[84:85]
	s_mov_b32 m0, s16
	ds_read_b128 v[178:181], v149 offset:49152
	ds_read_b128 v[182:185], v149 offset:50176
	ds_read_b128 v[186:189], v149 offset:51200
	ds_read_b128 v[198:201], v149 offset:52224
	ds_read_b128 v[202:205], v149 offset:53248
	ds_read_b128 v[206:209], v149 offset:54272
	ds_read_b128 v[210:213], v149 offset:55296
	ds_read_b128 v[214:217], v149 offset:56320
	global_load_lds_dwordx4 v[190:191], off
	s_add_i32 m0, s16, 0x2000
	s_add_u32 s14, s14, 0x40080
	v_lshl_add_u64 v[190:191], v[218:219], 0, s[84:85]
	s_addc_u32 s15, s15, 0
	s_add_i32 s16, s37, s18
	global_load_lds_dwordx4 v[190:191], off
	v_lshl_add_u64 v[190:191], s[14:15], 0, v[130:131]
	s_mov_b32 m0, s16
	s_nop 0
	global_load_lds_dwordx4 v[190:191], off
	v_lshl_add_u64 v[190:191], s[14:15], 0, v[132:133]
	s_add_i32 m0, s16, 0x2000
	s_nop 0
	global_load_lds_dwordx4 v[190:191], off
	v_lshl_add_u64 v[190:191], v[220:221], 0, s[84:85]
	s_mov_b32 m0, s23
	s_nop 0
	global_load_lds_dwordx4 v[190:191], off
	v_lshl_add_u64 v[190:191], v[222:223], 0, s[84:85]
	s_mov_b32 m0, s24
	s_nop 0
	global_load_lds_dwordx4 v[190:191], off
	s_waitcnt vmcnt(8)
	s_waitcnt lgkmcnt(0)
	s_barrier
	s_setprio 1
	s_waitcnt lgkmcnt(0)
	v_mfma_f32_16x16x32_bf16 v[62:65], v[142:145], v[178:181], v[62:65]
	v_mfma_f32_16x16x32_bf16 v[58:61], v[154:157], v[178:181], v[58:61]
	v_mfma_f32_16x16x32_bf16 v[46:49], v[142:145], v[186:189], v[46:49]
	v_mfma_f32_16x16x32_bf16 v[42:45], v[154:157], v[186:189], v[42:45]
	v_mfma_f32_16x16x32_bf16 v[30:33], v[142:145], v[202:205], v[30:33]
	v_mfma_f32_16x16x32_bf16 v[26:29], v[154:157], v[202:205], v[26:29]
	v_mfma_f32_16x16x32_bf16 v[14:17], v[142:145], v[210:213], v[14:17]
	v_mfma_f32_16x16x32_bf16 v[10:13], v[154:157], v[210:213], v[10:13]
	v_mfma_f32_16x16x32_bf16 v[62:65], v[150:153], v[182:185], v[62:65]
	v_mfma_f32_16x16x32_bf16 v[58:61], v[158:161], v[182:185], v[58:61]
	v_mfma_f32_16x16x32_bf16 v[46:49], v[150:153], v[198:201], v[46:49]
	v_mfma_f32_16x16x32_bf16 v[42:45], v[158:161], v[198:201], v[42:45]
	v_mfma_f32_16x16x32_bf16 v[30:33], v[150:153], v[206:209], v[30:33]
	v_mfma_f32_16x16x32_bf16 v[26:29], v[158:161], v[206:209], v[26:29]
	v_mfma_f32_16x16x32_bf16 v[14:17], v[150:153], v[214:217], v[14:17]
	v_mfma_f32_16x16x32_bf16 v[10:13], v[158:161], v[214:217], v[10:13]
	s_setprio 0
	s_setprio 1
	v_mfma_f32_16x16x32_bf16 v[54:57], v[162:165], v[178:181], v[54:57]
	v_mfma_f32_16x16x32_bf16 v[50:53], v[170:173], v[178:181], v[50:53]
	v_mfma_f32_16x16x32_bf16 v[38:41], v[162:165], v[186:189], v[38:41]
	v_mfma_f32_16x16x32_bf16 v[34:37], v[170:173], v[186:189], v[34:37]
	v_mfma_f32_16x16x32_bf16 v[22:25], v[162:165], v[202:205], v[22:25]
	v_mfma_f32_16x16x32_bf16 v[18:21], v[170:173], v[202:205], v[18:21]
	v_mfma_f32_16x16x32_bf16 v[6:9], v[162:165], v[210:213], v[6:9]
	v_mfma_f32_16x16x32_bf16 v[2:5], v[170:173], v[210:213], v[2:5]
	v_mfma_f32_16x16x32_bf16 v[54:57], v[166:169], v[182:185], v[54:57]
	v_mfma_f32_16x16x32_bf16 v[50:53], v[174:177], v[182:185], v[50:53]
	v_mfma_f32_16x16x32_bf16 v[38:41], v[166:169], v[198:201], v[38:41]
	v_mfma_f32_16x16x32_bf16 v[34:37], v[174:177], v[198:201], v[34:37]
	v_mfma_f32_16x16x32_bf16 v[22:25], v[166:169], v[206:209], v[22:25]
	v_mfma_f32_16x16x32_bf16 v[18:21], v[174:177], v[206:209], v[18:21]
	v_mfma_f32_16x16x32_bf16 v[6:9], v[166:169], v[214:217], v[6:9]
	v_mfma_f32_16x16x32_bf16 v[2:5], v[174:177], v[214:217], v[2:5]
	s_setprio 0
	s_barrier
	s_add_i32 s29, s29, 2
	s_add_u32 s12, s12, 0x100
	s_addc_u32 s13, s13, 0
	s_add_u32 s7, s7, 0x100
	s_addc_u32 s28, s28, 0
	s_cmp_gt_u32 s29, 13
	s_cbranch_scc0 .LBB0_213

.LBB0_997:
	s_add_u32 s16, s16, 0x40080
	s_addc_u32 s17, s17, 0
	s_add_u32 s11, s18, 0x100
	s_addc_u32 s36, s19, 0
	s_mov_b32 s37, -2
	s_add_u32 s18, s16, 0xfffc0080
	s_addc_u32 s19, s17, -1
	s_add_i32 s42, 0, 0x10000
	s_cmp_eq_u32 s37, 12
	s_cselect_b32 s21, s13, s19
	s_cselect_b32 s20, s12, s18
	s_cselect_b32 s19, s15, s36
	s_cselect_b32 s18, s14, s11
	s_add_i32 s46, 0, 0x14000
	v_add_u32_e32 v78, s42, v167
	v_add_u32_e32 v170, s46, v167
	ds_read_b128 v[66:69], v78
	ds_read_b128 v[70:73], v78 offset:1024
	ds_read_b128 v[74:77], v78 offset:2048
	ds_read_b128 v[78:81], v78 offset:3072
	ds_read_b128 v[154:157], v170
	ds_read_b128 v[158:161], v170 offset:1024
	ds_read_b128 v[162:165], v170 offset:2048
	ds_read_b128 v[170:173], v170 offset:3072
	v_lshl_add_u64 v[190:191], s[16:17], 0, v[150:151]
	s_add_i32 m0, s23, 0xc000
	ds_read_b128 v[174:177], v169
	ds_read_b128 v[178:181], v169 offset:1024
	ds_read_b128 v[182:185], v169 offset:2048
	ds_read_b128 v[186:189], v169 offset:3072
	ds_read_b128 v[198:201], v169 offset:4096
	ds_read_b128 v[202:205], v169 offset:5120
	ds_read_b128 v[206:209], v169 offset:6144
	ds_read_b128 v[210:213], v169 offset:7168
	global_load_lds_dwordx4 v[190:191], off
	v_lshl_add_u64 v[190:191], s[16:17], 0, v[152:153]
	s_add_i32 m0, s23, 0xe000
	s_nop 0
	global_load_lds_dwordx4 v[190:191], off
	s_waitcnt vmcnt(8)
	s_waitcnt lgkmcnt(0)
	s_barrier
	s_setprio 1
	s_waitcnt lgkmcnt(0)
	v_mfma_f32_16x16x32_bf16 v[144:147], v[66:69], v[174:177], 0
	v_mfma_f32_16x16x32_bf16 v[140:143], v[74:77], v[174:177], 0
	v_mfma_f32_16x16x32_bf16 v[136:139], v[66:69], v[182:185], 0
	v_mfma_f32_16x16x32_bf16 v[122:125], v[74:77], v[182:185], 0
	v_mfma_f32_16x16x32_bf16 v[118:121], v[66:69], v[198:201], 0
	v_mfma_f32_16x16x32_bf16 v[106:109], v[74:77], v[198:201], 0
	v_mfma_f32_16x16x32_bf16 v[102:105], v[66:69], v[206:209], 0
	v_mfma_f32_16x16x32_bf16 v[90:93], v[74:77], v[206:209], 0
	v_mfma_f32_16x16x32_bf16 v[144:147], v[70:73], v[178:181], v[144:147]
	v_mfma_f32_16x16x32_bf16 v[140:143], v[78:81], v[178:181], v[140:143]
	v_mfma_f32_16x16x32_bf16 v[136:139], v[70:73], v[186:189], v[136:139]
	v_mfma_f32_16x16x32_bf16 v[122:125], v[78:81], v[186:189], v[122:125]
	v_mfma_f32_16x16x32_bf16 v[118:121], v[70:73], v[202:205], v[118:121]
	v_mfma_f32_16x16x32_bf16 v[106:109], v[78:81], v[202:205], v[106:109]
	v_mfma_f32_16x16x32_bf16 v[102:105], v[70:73], v[210:213], v[102:105]
	v_mfma_f32_16x16x32_bf16 v[90:93], v[78:81], v[210:213], v[90:93]
	s_setprio 0
	s_setprio 1
	v_mfma_f32_16x16x32_bf16 v[132:135], v[154:157], v[174:177], 0
	v_mfma_f32_16x16x32_bf16 v[126:129], v[162:165], v[174:177], 0
	v_mfma_f32_16x16x32_bf16 v[114:117], v[154:157], v[182:185], 0
	v_mfma_f32_16x16x32_bf16 v[110:113], v[162:165], v[182:185], 0
	v_mfma_f32_16x16x32_bf16 v[98:101], v[154:157], v[198:201], 0
	v_mfma_f32_16x16x32_bf16 v[94:97], v[162:165], v[198:201], 0
	v_mfma_f32_16x16x32_bf16 v[86:89], v[154:157], v[206:209], 0
	v_mfma_f32_16x16x32_bf16 v[82:85], v[162:165], v[206:209], 0
	v_mfma_f32_16x16x32_bf16 v[132:135], v[158:161], v[178:181], v[132:135]
	v_mfma_f32_16x16x32_bf16 v[126:129], v[170:173], v[178:181], v[126:129]
	v_mfma_f32_16x16x32_bf16 v[114:117], v[158:161], v[186:189], v[114:117]
	v_mfma_f32_16x16x32_bf16 v[110:113], v[170:173], v[186:189], v[110:113]
	v_mfma_f32_16x16x32_bf16 v[98:101], v[158:161], v[202:205], v[98:101]
	v_mfma_f32_16x16x32_bf16 v[94:97], v[170:173], v[202:205], v[94:97]
	v_mfma_f32_16x16x32_bf16 v[86:89], v[158:161], v[210:213], v[86:89]
	v_mfma_f32_16x16x32_bf16 v[82:85], v[170:173], v[210:213], v[82:85]
	s_setprio 0
	s_barrier
	s_add_i32 s42, s42, s22
	v_lshl_add_u64 v[190:191], s[18:19], 0, v[130:131]
	s_mov_b32 m0, s42
	ds_read_b128 v[174:177], v169 offset:16384
	ds_read_b128 v[178:181], v169 offset:17408
	ds_read_b128 v[182:185], v169 offset:18432
	ds_read_b128 v[186:189], v169 offset:19456
	ds_read_b128 v[198:201], v169 offset:20480
	ds_read_b128 v[202:205], v169 offset:21504
	ds_read_b128 v[206:209], v169 offset:22528
	ds_read_b128 v[210:213], v169 offset:23552
	global_load_lds_dwordx4 v[190:191], off
	s_add_i32 m0, s42, 0x2000
	s_add_u32 s42, s18, 0x40000
	v_lshl_add_u64 v[214:215], s[18:19], 0, v[148:149]
	s_addc_u32 s43, s19, 0
	s_add_i32 s46, s46, s22
	global_load_lds_dwordx4 v[214:215], off
	v_lshl_add_u64 v[216:217], s[42:43], 0, v[130:131]
	s_mov_b32 m0, s46
	v_lshl_add_u64 v[218:219], s[20:21], 0, v[148:149]
	global_load_lds_dwordx4 v[216:217], off
	v_lshl_add_u64 v[216:217], s[42:43], 0, v[148:149]
	s_add_i32 m0, s46, 0x2000
	s_nop 0
	global_load_lds_dwordx4 v[216:217], off
	v_lshl_add_u64 v[216:217], s[20:21], 0, v[130:131]
	s_mov_b32 m0, s23
	s_nop 0
	global_load_lds_dwordx4 v[216:217], off
	s_mov_b32 m0, s24
	s_nop 0
	global_load_lds_dwordx4 v[218:219], off
	s_waitcnt vmcnt(8)
	s_waitcnt lgkmcnt(0)
	s_barrier
	s_setprio 1
	s_waitcnt lgkmcnt(0)
	v_mfma_f32_16x16x32_bf16 v[62:65], v[66:69], v[174:177], 0
	v_mfma_f32_16x16x32_bf16 v[58:61], v[74:77], v[174:177], 0
	v_mfma_f32_16x16x32_bf16 v[46:49], v[66:69], v[182:185], 0
	v_mfma_f32_16x16x32_bf16 v[42:45], v[74:77], v[182:185], 0
	v_mfma_f32_16x16x32_bf16 v[30:33], v[66:69], v[198:201], 0
	v_mfma_f32_16x16x32_bf16 v[26:29], v[74:77], v[198:201], 0
	v_mfma_f32_16x16x32_bf16 v[14:17], v[66:69], v[206:209], 0
	v_mfma_f32_16x16x32_bf16 v[10:13], v[74:77], v[206:209], 0
	v_mfma_f32_16x16x32_bf16 v[62:65], v[70:73], v[178:181], v[62:65]
	v_mfma_f32_16x16x32_bf16 v[58:61], v[78:81], v[178:181], v[58:61]
	v_mfma_f32_16x16x32_bf16 v[46:49], v[70:73], v[186:189], v[46:49]
	v_mfma_f32_16x16x32_bf16 v[42:45], v[78:81], v[186:189], v[42:45]
	v_mfma_f32_16x16x32_bf16 v[30:33], v[70:73], v[202:205], v[30:33]
	v_mfma_f32_16x16x32_bf16 v[26:29], v[78:81], v[202:205], v[26:29]
	v_mfma_f32_16x16x32_bf16 v[14:17], v[70:73], v[210:213], v[14:17]
	v_mfma_f32_16x16x32_bf16 v[10:13], v[78:81], v[210:213], v[10:13]
	s_setprio 0
	s_setprio 1
	v_mfma_f32_16x16x32_bf16 v[54:57], v[154:157], v[174:177], 0
	v_mfma_f32_16x16x32_bf16 v[50:53], v[162:165], v[174:177], 0
	v_mfma_f32_16x16x32_bf16 v[38:41], v[154:157], v[182:185], 0
	v_mfma_f32_16x16x32_bf16 v[34:37], v[162:165], v[182:185], 0
	v_mfma_f32_16x16x32_bf16 v[22:25], v[154:157], v[198:201], 0
	v_mfma_f32_16x16x32_bf16 v[18:21], v[162:165], v[198:201], 0
	v_mfma_f32_16x16x32_bf16 v[6:9], v[154:157], v[206:209], 0
	v_mfma_f32_16x16x32_bf16 v[2:5], v[162:165], v[206:209], 0
	v_mfma_f32_16x16x32_bf16 v[54:57], v[158:161], v[178:181], v[54:57]
	v_mfma_f32_16x16x32_bf16 v[50:53], v[170:173], v[178:181], v[50:53]
	v_mfma_f32_16x16x32_bf16 v[38:41], v[158:161], v[186:189], v[38:41]
	v_mfma_f32_16x16x32_bf16 v[34:37], v[170:173], v[186:189], v[34:37]
	v_mfma_f32_16x16x32_bf16 v[22:25], v[158:161], v[202:205], v[22:25]
	v_mfma_f32_16x16x32_bf16 v[18:21], v[170:173], v[202:205], v[18:21]
	v_mfma_f32_16x16x32_bf16 v[6:9], v[158:161], v[210:213], v[6:9]
	v_mfma_f32_16x16x32_bf16 v[2:5], v[170:173], v[210:213], v[2:5]
	s_setprio 0
	s_barrier
	s_add_i32 s42, 0, 0x18000
	s_add_i32 s43, 0, 0x1c000
	v_add_u32_e32 v78, s42, v167
	v_add_u32_e32 v170, s43, v167
	ds_read_b128 v[66:69], v78
	ds_read_b128 v[70:73], v78 offset:1024
	ds_read_b128 v[74:77], v78 offset:2048
	ds_read_b128 v[78:81], v78 offset:3072
	ds_read_b128 v[154:157], v170
	ds_read_b128 v[158:161], v170 offset:1024
	ds_read_b128 v[162:165], v170 offset:2048
	ds_read_b128 v[170:173], v170 offset:3072
	s_add_u32 s20, s20, 0x40000
	s_addc_u32 s21, s21, 0
	s_mov_b32 m0, s25
	v_lshl_add_u64 v[220:221], s[20:21], 0, v[130:131]
	ds_read_b128 v[174:177], v169 offset:32768
	ds_read_b128 v[178:181], v169 offset:33792
	ds_read_b128 v[182:185], v169 offset:34816
	ds_read_b128 v[186:189], v169 offset:35840
	ds_read_b128 v[198:201], v169 offset:36864
	ds_read_b128 v[202:205], v169 offset:37888
	ds_read_b128 v[206:209], v169 offset:38912
	ds_read_b128 v[210:213], v169 offset:39936
	global_load_lds_dwordx4 v[220:221], off
	v_lshl_add_u64 v[220:221], s[20:21], 0, v[148:149]
	s_mov_b32 m0, s26
	s_nop 0
	global_load_lds_dwordx4 v[220:221], off
	s_waitcnt vmcnt(8)
	s_waitcnt lgkmcnt(0)
	s_barrier
	s_setprio 1
	s_waitcnt lgkmcnt(0)
	v_mfma_f32_16x16x32_bf16 v[144:147], v[66:69], v[174:177], v[144:147]
	v_mfma_f32_16x16x32_bf16 v[140:143], v[74:77], v[174:177], v[140:143]
	v_mfma_f32_16x16x32_bf16 v[136:139], v[66:69], v[182:185], v[136:139]
	v_mfma_f32_16x16x32_bf16 v[122:125], v[74:77], v[182:185], v[122:125]
	v_mfma_f32_16x16x32_bf16 v[118:121], v[66:69], v[198:201], v[118:121]
	v_mfma_f32_16x16x32_bf16 v[106:109], v[74:77], v[198:201], v[106:109]
	v_mfma_f32_16x16x32_bf16 v[102:105], v[66:69], v[206:209], v[102:105]
	v_mfma_f32_16x16x32_bf16 v[90:93], v[74:77], v[206:209], v[90:93]
	v_mfma_f32_16x16x32_bf16 v[144:147], v[70:73], v[178:181], v[144:147]
	v_mfma_f32_16x16x32_bf16 v[140:143], v[78:81], v[178:181], v[140:143]
	v_mfma_f32_16x16x32_bf16 v[136:139], v[70:73], v[186:189], v[136:139]
	v_mfma_f32_16x16x32_bf16 v[122:125], v[78:81], v[186:189], v[122:125]
	v_mfma_f32_16x16x32_bf16 v[118:121], v[70:73], v[202:205], v[118:121]
	v_mfma_f32_16x16x32_bf16 v[106:109], v[78:81], v[202:205], v[106:109]
	v_mfma_f32_16x16x32_bf16 v[102:105], v[70:73], v[210:213], v[102:105]
	v_mfma_f32_16x16x32_bf16 v[90:93], v[78:81], v[210:213], v[90:93]
	s_setprio 0
	s_setprio 1
	v_mfma_f32_16x16x32_bf16 v[132:135], v[154:157], v[174:177], v[132:135]
	v_mfma_f32_16x16x32_bf16 v[126:129], v[162:165], v[174:177], v[126:129]
	v_mfma_f32_16x16x32_bf16 v[114:117], v[154:157], v[182:185], v[114:117]
	v_mfma_f32_16x16x32_bf16 v[110:113], v[162:165], v[182:185], v[110:113]
	v_mfma_f32_16x16x32_bf16 v[98:101], v[154:157], v[198:201], v[98:101]
	v_mfma_f32_16x16x32_bf16 v[94:97], v[162:165], v[198:201], v[94:97]
	v_mfma_f32_16x16x32_bf16 v[86:89], v[154:157], v[206:209], v[86:89]
	v_mfma_f32_16x16x32_bf16 v[82:85], v[162:165], v[206:209], v[82:85]
	v_mfma_f32_16x16x32_bf16 v[132:135], v[158:161], v[178:181], v[132:135]
	v_mfma_f32_16x16x32_bf16 v[126:129], v[170:173], v[178:181], v[126:129]
	v_mfma_f32_16x16x32_bf16 v[114:117], v[158:161], v[186:189], v[114:117]
	v_mfma_f32_16x16x32_bf16 v[110:113], v[170:173], v[186:189], v[110:113]
	v_mfma_f32_16x16x32_bf16 v[98:101], v[158:161], v[202:205], v[98:101]
	v_mfma_f32_16x16x32_bf16 v[94:97], v[170:173], v[202:205], v[94:97]
	v_mfma_f32_16x16x32_bf16 v[86:89], v[158:161], v[210:213], v[86:89]
	v_mfma_f32_16x16x32_bf16 v[82:85], v[170:173], v[210:213], v[82:85]
	s_setprio 0
	s_barrier
	s_add_i32 s20, s42, s22
	v_lshl_add_u64 v[190:191], v[190:191], 0, s[84:85]
	s_mov_b32 m0, s20
	ds_read_b128 v[174:177], v169 offset:49152
	ds_read_b128 v[178:181], v169 offset:50176
	ds_read_b128 v[182:185], v169 offset:51200
	ds_read_b128 v[186:189], v169 offset:52224
	ds_read_b128 v[198:201], v169 offset:53248
	ds_read_b128 v[202:205], v169 offset:54272
	ds_read_b128 v[206:209], v169 offset:55296
	ds_read_b128 v[210:213], v169 offset:56320
	global_load_lds_dwordx4 v[190:191], off
	s_add_i32 m0, s20, 0x2000
	s_add_u32 s18, s18, 0x40080
	v_lshl_add_u64 v[190:191], v[214:215], 0, s[84:85]
	s_addc_u32 s19, s19, 0
	s_add_i32 s20, s43, s22
	global_load_lds_dwordx4 v[190:191], off
	v_lshl_add_u64 v[190:191], s[18:19], 0, v[130:131]
	s_mov_b32 m0, s20
	s_nop 0
	global_load_lds_dwordx4 v[190:191], off
	v_lshl_add_u64 v[190:191], s[18:19], 0, v[148:149]
	s_add_i32 m0, s20, 0x2000
	s_nop 0
	global_load_lds_dwordx4 v[190:191], off
	v_lshl_add_u64 v[190:191], v[216:217], 0, s[84:85]
	s_mov_b32 m0, s27
	s_nop 0
	global_load_lds_dwordx4 v[190:191], off
	v_lshl_add_u64 v[190:191], v[218:219], 0, s[84:85]
	s_mov_b32 m0, s28
	s_nop 0
	global_load_lds_dwordx4 v[190:191], off
	s_waitcnt vmcnt(8)
	s_waitcnt lgkmcnt(0)
	s_barrier
	s_setprio 1
	s_waitcnt lgkmcnt(0)
	v_mfma_f32_16x16x32_bf16 v[62:65], v[66:69], v[174:177], v[62:65]
	v_mfma_f32_16x16x32_bf16 v[58:61], v[74:77], v[174:177], v[58:61]
	v_mfma_f32_16x16x32_bf16 v[46:49], v[66:69], v[182:185], v[46:49]
	v_mfma_f32_16x16x32_bf16 v[42:45], v[74:77], v[182:185], v[42:45]
	v_mfma_f32_16x16x32_bf16 v[30:33], v[66:69], v[198:201], v[30:33]
	v_mfma_f32_16x16x32_bf16 v[26:29], v[74:77], v[198:201], v[26:29]
	v_mfma_f32_16x16x32_bf16 v[14:17], v[66:69], v[206:209], v[14:17]
	v_mfma_f32_16x16x32_bf16 v[10:13], v[74:77], v[206:209], v[10:13]
	v_mfma_f32_16x16x32_bf16 v[62:65], v[70:73], v[178:181], v[62:65]
	v_mfma_f32_16x16x32_bf16 v[58:61], v[78:81], v[178:181], v[58:61]
	v_mfma_f32_16x16x32_bf16 v[46:49], v[70:73], v[186:189], v[46:49]
	v_mfma_f32_16x16x32_bf16 v[42:45], v[78:81], v[186:189], v[42:45]
	v_mfma_f32_16x16x32_bf16 v[30:33], v[70:73], v[202:205], v[30:33]
	v_mfma_f32_16x16x32_bf16 v[26:29], v[78:81], v[202:205], v[26:29]
	v_mfma_f32_16x16x32_bf16 v[14:17], v[70:73], v[210:213], v[14:17]
	v_mfma_f32_16x16x32_bf16 v[10:13], v[78:81], v[210:213], v[10:13]
	s_setprio 0
	s_setprio 1
	v_mfma_f32_16x16x32_bf16 v[54:57], v[154:157], v[174:177], v[54:57]
	v_mfma_f32_16x16x32_bf16 v[50:53], v[162:165], v[174:177], v[50:53]
	v_mfma_f32_16x16x32_bf16 v[38:41], v[154:157], v[182:185], v[38:41]
	v_mfma_f32_16x16x32_bf16 v[34:37], v[162:165], v[182:185], v[34:37]
	v_mfma_f32_16x16x32_bf16 v[22:25], v[154:157], v[198:201], v[22:25]
	v_mfma_f32_16x16x32_bf16 v[18:21], v[162:165], v[198:201], v[18:21]
	v_mfma_f32_16x16x32_bf16 v[6:9], v[154:157], v[206:209], v[6:9]
	v_mfma_f32_16x16x32_bf16 v[2:5], v[162:165], v[206:209], v[2:5]
	v_mfma_f32_16x16x32_bf16 v[54:57], v[158:161], v[178:181], v[54:57]
	v_mfma_f32_16x16x32_bf16 v[50:53], v[170:173], v[178:181], v[50:53]
	v_mfma_f32_16x16x32_bf16 v[38:41], v[158:161], v[186:189], v[38:41]
	v_mfma_f32_16x16x32_bf16 v[34:37], v[170:173], v[186:189], v[34:37]
	v_mfma_f32_16x16x32_bf16 v[22:25], v[158:161], v[202:205], v[22:25]
	v_mfma_f32_16x16x32_bf16 v[18:21], v[170:173], v[202:205], v[18:21]
	v_mfma_f32_16x16x32_bf16 v[6:9], v[158:161], v[210:213], v[6:9]
	v_mfma_f32_16x16x32_bf16 v[2:5], v[170:173], v[210:213], v[2:5]
	s_setprio 0
	s_barrier
	s_add_i32 s37, s37, 2
	s_add_u32 s16, s16, 0x100
	s_addc_u32 s17, s17, 0
	s_add_u32 s11, s11, 0x100
	s_addc_u32 s36, s36, 0
	s_cmp_gt_u32 s37, 13
	s_cbranch_scc0 .LBB0_998

.LBB0_1327:
	v_mov_b32_e32 v139, v131
	v_mov_b32_e32 v137, v131
	s_add_u32 s9, s12, 0x100
	v_lshl_add_u64 v[144:145], s[40:41], 0, v[136:137]
	v_lshl_add_u64 v[146:147], s[40:41], 0, v[138:139]
	s_addc_u32 s31, s13, 0
	s_mov_b32 s34, -2
	s_mov_b64 s[0:1], 0
	s_add_u32 s12, s92, s0
	s_addc_u32 s13, s93, s1
	s_add_u32 s14, s12, 0x48db700
	s_addc_u32 s15, s13, 0
	s_add_u32 s35, s9, s0
	s_addc_u32 s38, s31, s1
	s_add_i32 s39, 0, 0x10000
	s_cmpk_eq_i32 s0, 0x700
	s_cselect_b64 vcc, -1, 0
	s_and_b64 s[12:13], vcc, exec
	s_cselect_b32 s15, s91, s15
	s_cselect_b32 s14, s90, s14
	v_add_u32_e32 v130, s39, v154
	s_cselect_b32 s13, s11, s38
	s_cselect_b32 s12, s10, s35
	s_add_i32 s35, 0, 0x14000
	ds_read_b128 v[160:163], v130
	ds_read_b128 v[164:167], v130 offset:1024
	ds_read_b128 v[168:171], v130 offset:2048
	ds_read_b128 v[172:175], v130 offset:3072
	v_add_u32_e32 v130, s35, v154
	ds_read_b128 v[176:179], v130
	ds_read_b128 v[180:183], v130 offset:1024
	ds_read_b128 v[184:187], v130 offset:2048
	ds_read_b128 v[188:191], v130 offset:3072
	v_lshl_add_u64 v[230:231], v[146:147], 0, s[0:1]
	s_add_i32 m0, s21, 0xc000
	ds_read_b128 v[198:201], v143
	ds_read_b128 v[202:205], v143 offset:1024
	ds_read_b128 v[206:209], v143 offset:2048
	ds_read_b128 v[210:213], v143 offset:3072
	ds_read_b128 v[214:217], v143 offset:4096
	ds_read_b128 v[218:221], v143 offset:5120
	ds_read_b128 v[222:225], v143 offset:6144
	ds_read_b128 v[236:239], v143 offset:7168
	global_load_lds_dwordx4 v[230:231], off
	v_lshl_add_u64 v[230:231], v[144:145], 0, s[0:1]
	s_add_i32 m0, s21, 0xe000
	s_nop 0
	global_load_lds_dwordx4 v[230:231], off
	s_waitcnt vmcnt(8)
	s_waitcnt lgkmcnt(0)
	s_barrier
	s_setprio 1
	s_waitcnt lgkmcnt(0)
	v_mfma_f32_16x16x32_bf16 v[126:129], v[160:163], v[198:201], 0
	v_mfma_f32_16x16x32_bf16 v[118:121], v[168:171], v[198:201], 0
	v_mfma_f32_16x16x32_bf16 v[110:113], v[160:163], v[206:209], 0
	v_mfma_f32_16x16x32_bf16 v[102:105], v[168:171], v[206:209], 0
	v_mfma_f32_16x16x32_bf16 v[94:97], v[160:163], v[214:217], 0
	v_mfma_f32_16x16x32_bf16 v[86:89], v[168:171], v[214:217], 0
	v_mfma_f32_16x16x32_bf16 v[78:81], v[160:163], v[222:225], 0
	v_mfma_f32_16x16x32_bf16 v[70:73], v[168:171], v[222:225], 0
	v_mfma_f32_16x16x32_bf16 v[126:129], v[164:167], v[202:205], v[126:129]
	v_mfma_f32_16x16x32_bf16 v[118:121], v[172:175], v[202:205], v[118:121]
	v_mfma_f32_16x16x32_bf16 v[110:113], v[164:167], v[210:213], v[110:113]
	v_mfma_f32_16x16x32_bf16 v[102:105], v[172:175], v[210:213], v[102:105]
	v_mfma_f32_16x16x32_bf16 v[94:97], v[164:167], v[218:221], v[94:97]
	v_mfma_f32_16x16x32_bf16 v[86:89], v[172:175], v[218:221], v[86:89]
	v_mfma_f32_16x16x32_bf16 v[78:81], v[164:167], v[236:239], v[78:81]
	v_mfma_f32_16x16x32_bf16 v[70:73], v[172:175], v[236:239], v[70:73]
	s_setprio 0
	s_setprio 1
	v_mfma_f32_16x16x32_bf16 v[122:125], v[176:179], v[198:201], 0
	v_mfma_f32_16x16x32_bf16 v[114:117], v[184:187], v[198:201], 0
	v_mfma_f32_16x16x32_bf16 v[106:109], v[176:179], v[206:209], 0
	v_mfma_f32_16x16x32_bf16 v[98:101], v[184:187], v[206:209], 0
	v_mfma_f32_16x16x32_bf16 v[90:93], v[176:179], v[214:217], 0
	v_mfma_f32_16x16x32_bf16 v[82:85], v[184:187], v[214:217], 0
	v_mfma_f32_16x16x32_bf16 v[74:77], v[176:179], v[222:225], 0
	v_mfma_f32_16x16x32_bf16 v[66:69], v[184:187], v[222:225], 0
	v_mfma_f32_16x16x32_bf16 v[122:125], v[180:183], v[202:205], v[122:125]
	v_mfma_f32_16x16x32_bf16 v[114:117], v[188:191], v[202:205], v[114:117]
	v_mfma_f32_16x16x32_bf16 v[106:109], v[180:183], v[210:213], v[106:109]
	v_mfma_f32_16x16x32_bf16 v[98:101], v[188:191], v[210:213], v[98:101]
	v_mfma_f32_16x16x32_bf16 v[90:93], v[180:183], v[218:221], v[90:93]
	v_mfma_f32_16x16x32_bf16 v[82:85], v[188:191], v[218:221], v[82:85]
	v_mfma_f32_16x16x32_bf16 v[74:77], v[180:183], v[236:239], v[74:77]
	v_mfma_f32_16x16x32_bf16 v[66:69], v[188:191], v[236:239], v[66:69]
	s_setprio 0
	s_barrier
	s_add_i32 s38, s39, s16
	v_lshl_add_u64 v[230:231], s[12:13], 0, v[134:135]
	s_mov_b32 m0, s38
	ds_read_b128 v[198:201], v143 offset:16384
	ds_read_b128 v[202:205], v143 offset:17408
	ds_read_b128 v[206:209], v143 offset:18432
	ds_read_b128 v[210:213], v143 offset:19456
	ds_read_b128 v[214:217], v143 offset:20480
	ds_read_b128 v[218:221], v143 offset:21504
	ds_read_b128 v[222:225], v143 offset:22528
	ds_read_b128 v[236:239], v143 offset:23552
	global_load_lds_dwordx4 v[230:231], off
	s_add_i32 m0, s38, 0x2000
	s_add_u32 s38, s12, 0x40000
	v_lshl_add_u64 v[242:243], s[12:13], 0, v[132:133]
	s_addc_u32 s39, s13, 0
	s_add_i32 s35, s35, s16
	global_load_lds_dwordx4 v[242:243], off
	v_lshl_add_u64 v[244:245], s[38:39], 0, v[134:135]
	s_mov_b32 m0, s35
	v_cndmask_b32_e32 v130, v142, v155, vcc
	global_load_lds_dwordx4 v[244:245], off
	v_lshl_add_u64 v[244:245], s[38:39], 0, v[132:133]
	s_add_i32 m0, s35, 0x2000
	s_nop 0
	global_load_lds_dwordx4 v[244:245], off
	s_mov_b32 m0, s21
	v_lshl_add_u64 v[244:245], s[14:15], 0, v[130:131]
	global_load_lds_dwordx4 v130, s[14:15]
	v_cndmask_b32_e32 v130, v140, v156, vcc
	s_mov_b32 m0, s23
	v_lshl_add_u64 v[246:247], s[14:15], 0, v[130:131]
	global_load_lds_dwordx4 v130, s[14:15]
	s_waitcnt vmcnt(8)
	s_waitcnt lgkmcnt(0)
	s_barrier
	s_setprio 1
	s_waitcnt lgkmcnt(0)
	v_mfma_f32_16x16x32_bf16 v[62:65], v[160:163], v[198:201], 0
	v_mfma_f32_16x16x32_bf16 v[54:57], v[168:171], v[198:201], 0
	v_mfma_f32_16x16x32_bf16 v[46:49], v[160:163], v[206:209], 0
	v_mfma_f32_16x16x32_bf16 v[38:41], v[168:171], v[206:209], 0
	v_mfma_f32_16x16x32_bf16 v[30:33], v[160:163], v[214:217], 0
	v_mfma_f32_16x16x32_bf16 v[22:25], v[168:171], v[214:217], 0
	v_mfma_f32_16x16x32_bf16 v[14:17], v[160:163], v[222:225], 0
	v_mfma_f32_16x16x32_bf16 v[6:9], v[168:171], v[222:225], 0
	v_mfma_f32_16x16x32_bf16 v[62:65], v[164:167], v[202:205], v[62:65]
	v_mfma_f32_16x16x32_bf16 v[54:57], v[172:175], v[202:205], v[54:57]
	v_mfma_f32_16x16x32_bf16 v[46:49], v[164:167], v[210:213], v[46:49]
	v_mfma_f32_16x16x32_bf16 v[38:41], v[172:175], v[210:213], v[38:41]
	v_mfma_f32_16x16x32_bf16 v[30:33], v[164:167], v[218:221], v[30:33]
	v_mfma_f32_16x16x32_bf16 v[22:25], v[172:175], v[218:221], v[22:25]
	v_mfma_f32_16x16x32_bf16 v[14:17], v[164:167], v[236:239], v[14:17]
	v_mfma_f32_16x16x32_bf16 v[6:9], v[172:175], v[236:239], v[6:9]
	s_setprio 0
	s_setprio 1
	v_mfma_f32_16x16x32_bf16 v[58:61], v[176:179], v[198:201], 0
	v_mfma_f32_16x16x32_bf16 v[50:53], v[184:187], v[198:201], 0
	v_mfma_f32_16x16x32_bf16 v[42:45], v[176:179], v[206:209], 0
	v_mfma_f32_16x16x32_bf16 v[34:37], v[184:187], v[206:209], 0
	v_mfma_f32_16x16x32_bf16 v[26:29], v[176:179], v[214:217], 0
	v_mfma_f32_16x16x32_bf16 v[18:21], v[184:187], v[214:217], 0
	v_mfma_f32_16x16x32_bf16 v[10:13], v[176:179], v[222:225], 0
	v_mfma_f32_16x16x32_bf16 v[2:5], v[184:187], v[222:225], 0
	v_mfma_f32_16x16x32_bf16 v[58:61], v[180:183], v[202:205], v[58:61]
	v_mfma_f32_16x16x32_bf16 v[50:53], v[188:191], v[202:205], v[50:53]
	v_mfma_f32_16x16x32_bf16 v[42:45], v[180:183], v[210:213], v[42:45]
	v_mfma_f32_16x16x32_bf16 v[34:37], v[188:191], v[210:213], v[34:37]
	v_mfma_f32_16x16x32_bf16 v[26:29], v[180:183], v[218:221], v[26:29]
	v_mfma_f32_16x16x32_bf16 v[18:21], v[188:191], v[218:221], v[18:21]
	v_mfma_f32_16x16x32_bf16 v[10:13], v[180:183], v[236:239], v[10:13]
	v_mfma_f32_16x16x32_bf16 v[2:5], v[188:191], v[236:239], v[2:5]
	s_setprio 0
	s_barrier
	s_add_i32 s35, 0, 0x18000
	v_add_u32_e32 v130, s35, v154
	s_add_i32 s38, 0, 0x1c000
	ds_read_b128 v[160:163], v130
	ds_read_b128 v[164:167], v130 offset:1024
	ds_read_b128 v[168:171], v130 offset:2048
	ds_read_b128 v[172:175], v130 offset:3072
	v_add_u32_e32 v130, s38, v154
	ds_read_b128 v[176:179], v130
	ds_read_b128 v[180:183], v130 offset:1024
	ds_read_b128 v[184:187], v130 offset:2048
	ds_read_b128 v[188:191], v130 offset:3072
	s_mov_b32 m0, s24
	v_cndmask_b32_e32 v130, v138, v157, vcc
	ds_read_b128 v[198:201], v143 offset:32768
	ds_read_b128 v[202:205], v143 offset:33792
	ds_read_b128 v[206:209], v143 offset:34816
	ds_read_b128 v[210:213], v143 offset:35840
	ds_read_b128 v[214:217], v143 offset:36864
	ds_read_b128 v[218:221], v143 offset:37888
	ds_read_b128 v[222:225], v143 offset:38912
	ds_read_b128 v[236:239], v143 offset:39936
	global_load_lds_dwordx4 v130, s[14:15]
	v_cndmask_b32_e32 v130, v136, v158, vcc
	s_mov_b32 m0, s25
	s_nop 0
	global_load_lds_dwordx4 v130, s[14:15]
	s_waitcnt vmcnt(8)
	s_waitcnt lgkmcnt(0)
	s_barrier
	s_setprio 1
	s_waitcnt lgkmcnt(0)
	v_mfma_f32_16x16x32_bf16 v[126:129], v[160:163], v[198:201], v[126:129]
	v_mfma_f32_16x16x32_bf16 v[118:121], v[168:171], v[198:201], v[118:121]
	v_mfma_f32_16x16x32_bf16 v[110:113], v[160:163], v[206:209], v[110:113]
	v_mfma_f32_16x16x32_bf16 v[102:105], v[168:171], v[206:209], v[102:105]
	v_mfma_f32_16x16x32_bf16 v[94:97], v[160:163], v[214:217], v[94:97]
	v_mfma_f32_16x16x32_bf16 v[86:89], v[168:171], v[214:217], v[86:89]
	v_mfma_f32_16x16x32_bf16 v[78:81], v[160:163], v[222:225], v[78:81]
	v_mfma_f32_16x16x32_bf16 v[70:73], v[168:171], v[222:225], v[70:73]
	v_mfma_f32_16x16x32_bf16 v[126:129], v[164:167], v[202:205], v[126:129]
	v_mfma_f32_16x16x32_bf16 v[118:121], v[172:175], v[202:205], v[118:121]
	v_mfma_f32_16x16x32_bf16 v[110:113], v[164:167], v[210:213], v[110:113]
	v_mfma_f32_16x16x32_bf16 v[102:105], v[172:175], v[210:213], v[102:105]
	v_mfma_f32_16x16x32_bf16 v[94:97], v[164:167], v[218:221], v[94:97]
	v_mfma_f32_16x16x32_bf16 v[86:89], v[172:175], v[218:221], v[86:89]
	v_mfma_f32_16x16x32_bf16 v[78:81], v[164:167], v[236:239], v[78:81]
	v_mfma_f32_16x16x32_bf16 v[70:73], v[172:175], v[236:239], v[70:73]
	s_setprio 0
	s_setprio 1
	v_mfma_f32_16x16x32_bf16 v[122:125], v[176:179], v[198:201], v[122:125]
	v_mfma_f32_16x16x32_bf16 v[114:117], v[184:187], v[198:201], v[114:117]
	v_mfma_f32_16x16x32_bf16 v[106:109], v[176:179], v[206:209], v[106:109]
	v_mfma_f32_16x16x32_bf16 v[98:101], v[184:187], v[206:209], v[98:101]
	v_mfma_f32_16x16x32_bf16 v[90:93], v[176:179], v[214:217], v[90:93]
	v_mfma_f32_16x16x32_bf16 v[82:85], v[184:187], v[214:217], v[82:85]
	v_mfma_f32_16x16x32_bf16 v[74:77], v[176:179], v[222:225], v[74:77]
	v_mfma_f32_16x16x32_bf16 v[66:69], v[184:187], v[222:225], v[66:69]
	v_mfma_f32_16x16x32_bf16 v[122:125], v[180:183], v[202:205], v[122:125]
	v_mfma_f32_16x16x32_bf16 v[114:117], v[188:191], v[202:205], v[114:117]
	v_mfma_f32_16x16x32_bf16 v[106:109], v[180:183], v[210:213], v[106:109]
	v_mfma_f32_16x16x32_bf16 v[98:101], v[188:191], v[210:213], v[98:101]
	v_mfma_f32_16x16x32_bf16 v[90:93], v[180:183], v[218:221], v[90:93]
	v_mfma_f32_16x16x32_bf16 v[82:85], v[188:191], v[218:221], v[82:85]
	v_mfma_f32_16x16x32_bf16 v[74:77], v[180:183], v[236:239], v[74:77]
	v_mfma_f32_16x16x32_bf16 v[66:69], v[188:191], v[236:239], v[66:69]
	s_setprio 0
	s_barrier
	s_add_i32 s14, s35, s16
	v_lshl_add_u64 v[230:231], v[230:231], 0, s[84:85]
	s_mov_b32 m0, s14
	ds_read_b128 v[198:201], v143 offset:49152
	ds_read_b128 v[202:205], v143 offset:50176
	ds_read_b128 v[206:209], v143 offset:51200
	ds_read_b128 v[210:213], v143 offset:52224
	ds_read_b128 v[214:217], v143 offset:53248
	ds_read_b128 v[218:221], v143 offset:54272
	ds_read_b128 v[222:225], v143 offset:55296
	ds_read_b128 v[236:239], v143 offset:56320
	global_load_lds_dwordx4 v[230:231], off
	s_add_i32 m0, s14, 0x2000
	s_add_u32 s12, s12, 0x40080
	v_lshl_add_u64 v[230:231], v[242:243], 0, s[84:85]
	s_addc_u32 s13, s13, 0
	s_add_i32 s14, s38, s16
	global_load_lds_dwordx4 v[230:231], off
	v_lshl_add_u64 v[230:231], s[12:13], 0, v[134:135]
	s_mov_b32 m0, s14
	s_nop 0
	global_load_lds_dwordx4 v[230:231], off
	v_lshl_add_u64 v[230:231], s[12:13], 0, v[132:133]
	s_add_i32 m0, s14, 0x2000
	s_nop 0
	global_load_lds_dwordx4 v[230:231], off
	v_lshl_add_u64 v[230:231], v[244:245], 0, s[84:85]
	s_mov_b32 m0, s26
	s_nop 0
	global_load_lds_dwordx4 v[230:231], off
	v_lshl_add_u64 v[230:231], v[246:247], 0, s[84:85]
	s_mov_b32 m0, s27
	s_nop 0
	global_load_lds_dwordx4 v[230:231], off
	s_waitcnt vmcnt(8)
	s_waitcnt lgkmcnt(0)
	s_barrier
	s_setprio 1
	s_waitcnt lgkmcnt(0)
	v_mfma_f32_16x16x32_bf16 v[62:65], v[160:163], v[198:201], v[62:65]
	v_mfma_f32_16x16x32_bf16 v[54:57], v[168:171], v[198:201], v[54:57]
	v_mfma_f32_16x16x32_bf16 v[46:49], v[160:163], v[206:209], v[46:49]
	v_mfma_f32_16x16x32_bf16 v[38:41], v[168:171], v[206:209], v[38:41]
	v_mfma_f32_16x16x32_bf16 v[30:33], v[160:163], v[214:217], v[30:33]
	v_mfma_f32_16x16x32_bf16 v[22:25], v[168:171], v[214:217], v[22:25]
	v_mfma_f32_16x16x32_bf16 v[14:17], v[160:163], v[222:225], v[14:17]
	v_mfma_f32_16x16x32_bf16 v[6:9], v[168:171], v[222:225], v[6:9]
	v_mfma_f32_16x16x32_bf16 v[62:65], v[164:167], v[202:205], v[62:65]
	v_mfma_f32_16x16x32_bf16 v[54:57], v[172:175], v[202:205], v[54:57]
	v_mfma_f32_16x16x32_bf16 v[46:49], v[164:167], v[210:213], v[46:49]
	v_mfma_f32_16x16x32_bf16 v[38:41], v[172:175], v[210:213], v[38:41]
	v_mfma_f32_16x16x32_bf16 v[30:33], v[164:167], v[218:221], v[30:33]
	v_mfma_f32_16x16x32_bf16 v[22:25], v[172:175], v[218:221], v[22:25]
	v_mfma_f32_16x16x32_bf16 v[14:17], v[164:167], v[236:239], v[14:17]
	v_mfma_f32_16x16x32_bf16 v[6:9], v[172:175], v[236:239], v[6:9]
	s_setprio 0
	s_setprio 1
	v_mfma_f32_16x16x32_bf16 v[58:61], v[176:179], v[198:201], v[58:61]
	v_mfma_f32_16x16x32_bf16 v[50:53], v[184:187], v[198:201], v[50:53]
	v_mfma_f32_16x16x32_bf16 v[42:45], v[176:179], v[206:209], v[42:45]
	v_mfma_f32_16x16x32_bf16 v[34:37], v[184:187], v[206:209], v[34:37]
	v_mfma_f32_16x16x32_bf16 v[26:29], v[176:179], v[214:217], v[26:29]
	v_mfma_f32_16x16x32_bf16 v[18:21], v[184:187], v[214:217], v[18:21]
	v_mfma_f32_16x16x32_bf16 v[10:13], v[176:179], v[222:225], v[10:13]
	v_mfma_f32_16x16x32_bf16 v[2:5], v[184:187], v[222:225], v[2:5]
	v_mfma_f32_16x16x32_bf16 v[58:61], v[180:183], v[202:205], v[58:61]
	v_mfma_f32_16x16x32_bf16 v[50:53], v[188:191], v[202:205], v[50:53]
	v_mfma_f32_16x16x32_bf16 v[42:45], v[180:183], v[210:213], v[42:45]
	v_mfma_f32_16x16x32_bf16 v[34:37], v[188:191], v[210:213], v[34:37]
	v_mfma_f32_16x16x32_bf16 v[26:29], v[180:183], v[218:221], v[26:29]
	v_mfma_f32_16x16x32_bf16 v[18:21], v[188:191], v[218:221], v[18:21]
	v_mfma_f32_16x16x32_bf16 v[10:13], v[180:183], v[236:239], v[10:13]
	v_mfma_f32_16x16x32_bf16 v[2:5], v[188:191], v[236:239], v[2:5]
	s_setprio 0
	s_barrier
	s_add_i32 s34, s34, 2
	s_add_u32 s0, s0, 0x100
	s_addc_u32 s1, s1, 0
	s_cmp_gt_u32 s34, 13
	s_cbranch_scc0 .LBB0_1328

.LBB0_1396:
	s_add_u32 s18, s18, 0x80080
	s_addc_u32 s19, s19, 0
	s_add_u32 s9, s20, 0x100
	s_addc_u32 s11, s21, 0
	s_mov_b32 s38, -2
	s_add_u32 s20, s18, 0xfff80080
	s_addc_u32 s21, s19, -1
	s_add_i32 s39, 0, 0x10000
	s_cmp_eq_u32 s38, 28
	s_cselect_b32 s23, s13, s21
	s_cselect_b32 s22, s12, s20
	v_add_u32_e32 v142, s39, v145
	s_cselect_b32 s21, s17, s11
	s_cselect_b32 s20, s16, s9
	s_add_i32 s42, 0, 0x14000
	ds_read_b128 v[148:151], v142
	ds_read_b128 v[152:155], v142 offset:1024
	ds_read_b128 v[156:159], v142 offset:2048
	ds_read_b128 v[160:163], v142 offset:3072
	v_add_u32_e32 v142, s42, v145
	ds_read_b128 v[164:167], v142
	ds_read_b128 v[168:171], v142 offset:1024
	ds_read_b128 v[172:175], v142 offset:2048
	ds_read_b128 v[176:179], v142 offset:3072
	v_lshl_add_u64 v[142:143], s[18:19], 0, v[138:139]
	s_add_i32 m0, s15, 0xc000
	ds_read_b128 v[180:183], v147
	ds_read_b128 v[184:187], v147 offset:1024
	ds_read_b128 v[188:191], v147 offset:2048
	ds_read_b128 v[198:201], v147 offset:3072
	ds_read_b128 v[202:205], v147 offset:4096
	ds_read_b128 v[206:209], v147 offset:5120
	ds_read_b128 v[210:213], v147 offset:6144
	ds_read_b128 v[214:217], v147 offset:7168
	global_load_lds_dwordx4 v[142:143], off
	v_lshl_add_u64 v[142:143], s[18:19], 0, v[140:141]
	s_add_i32 m0, s15, 0xe000
	s_nop 0
	global_load_lds_dwordx4 v[142:143], off
	s_waitcnt vmcnt(8)
	s_waitcnt lgkmcnt(0)
	s_barrier
	s_setprio 1
	s_waitcnt lgkmcnt(0)
	v_mfma_f32_16x16x32_bf16 v[126:129], v[148:151], v[180:183], 0
	v_mfma_f32_16x16x32_bf16 v[122:125], v[156:159], v[180:183], 0
	v_mfma_f32_16x16x32_bf16 v[110:113], v[148:151], v[188:191], 0
	v_mfma_f32_16x16x32_bf16 v[106:109], v[156:159], v[188:191], 0
	v_mfma_f32_16x16x32_bf16 v[94:97], v[148:151], v[202:205], 0
	v_mfma_f32_16x16x32_bf16 v[90:93], v[156:159], v[202:205], 0
	v_mfma_f32_16x16x32_bf16 v[78:81], v[148:151], v[210:213], 0
	v_mfma_f32_16x16x32_bf16 v[74:77], v[156:159], v[210:213], 0
	v_mfma_f32_16x16x32_bf16 v[126:129], v[152:155], v[184:187], v[126:129]
	v_mfma_f32_16x16x32_bf16 v[122:125], v[160:163], v[184:187], v[122:125]
	v_mfma_f32_16x16x32_bf16 v[110:113], v[152:155], v[198:201], v[110:113]
	v_mfma_f32_16x16x32_bf16 v[106:109], v[160:163], v[198:201], v[106:109]
	v_mfma_f32_16x16x32_bf16 v[94:97], v[152:155], v[206:209], v[94:97]
	v_mfma_f32_16x16x32_bf16 v[90:93], v[160:163], v[206:209], v[90:93]
	v_mfma_f32_16x16x32_bf16 v[78:81], v[152:155], v[214:217], v[78:81]
	v_mfma_f32_16x16x32_bf16 v[74:77], v[160:163], v[214:217], v[74:77]
	s_setprio 0
	s_setprio 1
	v_mfma_f32_16x16x32_bf16 v[118:121], v[164:167], v[180:183], 0
	v_mfma_f32_16x16x32_bf16 v[114:117], v[172:175], v[180:183], 0
	v_mfma_f32_16x16x32_bf16 v[102:105], v[164:167], v[188:191], 0
	v_mfma_f32_16x16x32_bf16 v[98:101], v[172:175], v[188:191], 0
	v_mfma_f32_16x16x32_bf16 v[86:89], v[164:167], v[202:205], 0
	v_mfma_f32_16x16x32_bf16 v[82:85], v[172:175], v[202:205], 0
	v_mfma_f32_16x16x32_bf16 v[70:73], v[164:167], v[210:213], 0
	v_mfma_f32_16x16x32_bf16 v[66:69], v[172:175], v[210:213], 0
	v_mfma_f32_16x16x32_bf16 v[118:121], v[168:171], v[184:187], v[118:121]
	v_mfma_f32_16x16x32_bf16 v[114:117], v[176:179], v[184:187], v[114:117]
	v_mfma_f32_16x16x32_bf16 v[102:105], v[168:171], v[198:201], v[102:105]
	v_mfma_f32_16x16x32_bf16 v[98:101], v[176:179], v[198:201], v[98:101]
	v_mfma_f32_16x16x32_bf16 v[86:89], v[168:171], v[206:209], v[86:89]
	v_mfma_f32_16x16x32_bf16 v[82:85], v[176:179], v[206:209], v[82:85]
	v_mfma_f32_16x16x32_bf16 v[70:73], v[168:171], v[214:217], v[70:73]
	v_mfma_f32_16x16x32_bf16 v[66:69], v[176:179], v[214:217], v[66:69]
	s_setprio 0
	s_barrier
	s_add_i32 s39, s39, s26
	v_lshl_add_u64 v[142:143], s[20:21], 0, v[130:131]
	s_mov_b32 m0, s39
	ds_read_b128 v[180:183], v147 offset:16384
	ds_read_b128 v[184:187], v147 offset:17408
	ds_read_b128 v[188:191], v147 offset:18432
	ds_read_b128 v[198:201], v147 offset:19456
	ds_read_b128 v[202:205], v147 offset:20480
	ds_read_b128 v[206:209], v147 offset:21504
	ds_read_b128 v[210:213], v147 offset:22528
	ds_read_b128 v[214:217], v147 offset:23552
	global_load_lds_dwordx4 v[142:143], off
	s_add_i32 m0, s39, 0x2000
	s_add_u32 s40, s20, 0x80000
	v_lshl_add_u64 v[218:219], s[20:21], 0, v[132:133]
	s_addc_u32 s41, s21, 0
	s_add_i32 s39, s42, s26
	global_load_lds_dwordx4 v[218:219], off
	v_lshl_add_u64 v[220:221], s[40:41], 0, v[130:131]
	s_mov_b32 m0, s39
	v_lshl_add_u64 v[222:223], s[22:23], 0, v[134:135]
	global_load_lds_dwordx4 v[220:221], off
	v_lshl_add_u64 v[220:221], s[40:41], 0, v[132:133]
	s_add_i32 m0, s39, 0x2000
	s_nop 0
	global_load_lds_dwordx4 v[220:221], off
	v_lshl_add_u64 v[220:221], s[22:23], 0, v[136:137]
	s_mov_b32 m0, s15
	s_nop 0
	global_load_lds_dwordx4 v[220:221], off
	s_mov_b32 m0, s28
	s_nop 0
	global_load_lds_dwordx4 v[222:223], off
	s_waitcnt vmcnt(8)
	s_waitcnt lgkmcnt(0)
	s_barrier
	s_setprio 1
	s_waitcnt lgkmcnt(0)
	v_mfma_f32_16x16x32_bf16 v[62:65], v[148:151], v[180:183], 0
	v_mfma_f32_16x16x32_bf16 v[58:61], v[156:159], v[180:183], 0
	v_mfma_f32_16x16x32_bf16 v[46:49], v[148:151], v[188:191], 0
	v_mfma_f32_16x16x32_bf16 v[42:45], v[156:159], v[188:191], 0
	v_mfma_f32_16x16x32_bf16 v[30:33], v[148:151], v[202:205], 0
	v_mfma_f32_16x16x32_bf16 v[26:29], v[156:159], v[202:205], 0
	v_mfma_f32_16x16x32_bf16 v[14:17], v[148:151], v[210:213], 0
	v_mfma_f32_16x16x32_bf16 v[10:13], v[156:159], v[210:213], 0
	v_mfma_f32_16x16x32_bf16 v[62:65], v[152:155], v[184:187], v[62:65]
	v_mfma_f32_16x16x32_bf16 v[58:61], v[160:163], v[184:187], v[58:61]
	v_mfma_f32_16x16x32_bf16 v[46:49], v[152:155], v[198:201], v[46:49]
	v_mfma_f32_16x16x32_bf16 v[42:45], v[160:163], v[198:201], v[42:45]
	v_mfma_f32_16x16x32_bf16 v[30:33], v[152:155], v[206:209], v[30:33]
	v_mfma_f32_16x16x32_bf16 v[26:29], v[160:163], v[206:209], v[26:29]
	v_mfma_f32_16x16x32_bf16 v[14:17], v[152:155], v[214:217], v[14:17]
	v_mfma_f32_16x16x32_bf16 v[10:13], v[160:163], v[214:217], v[10:13]
	s_setprio 0
	s_setprio 1
	v_mfma_f32_16x16x32_bf16 v[54:57], v[164:167], v[180:183], 0
	v_mfma_f32_16x16x32_bf16 v[50:53], v[172:175], v[180:183], 0
	v_mfma_f32_16x16x32_bf16 v[38:41], v[164:167], v[188:191], 0
	v_mfma_f32_16x16x32_bf16 v[34:37], v[172:175], v[188:191], 0
	v_mfma_f32_16x16x32_bf16 v[22:25], v[164:167], v[202:205], 0
	v_mfma_f32_16x16x32_bf16 v[18:21], v[172:175], v[202:205], 0
	v_mfma_f32_16x16x32_bf16 v[6:9], v[164:167], v[210:213], 0
	v_mfma_f32_16x16x32_bf16 v[2:5], v[172:175], v[210:213], 0
	v_mfma_f32_16x16x32_bf16 v[54:57], v[168:171], v[184:187], v[54:57]
	v_mfma_f32_16x16x32_bf16 v[50:53], v[176:179], v[184:187], v[50:53]
	v_mfma_f32_16x16x32_bf16 v[38:41], v[168:171], v[198:201], v[38:41]
	v_mfma_f32_16x16x32_bf16 v[34:37], v[176:179], v[198:201], v[34:37]
	v_mfma_f32_16x16x32_bf16 v[22:25], v[168:171], v[206:209], v[22:25]
	v_mfma_f32_16x16x32_bf16 v[18:21], v[176:179], v[206:209], v[18:21]
	v_mfma_f32_16x16x32_bf16 v[6:9], v[168:171], v[214:217], v[6:9]
	v_mfma_f32_16x16x32_bf16 v[2:5], v[176:179], v[214:217], v[2:5]
	s_setprio 0
	s_barrier
	s_add_i32 s39, 0, 0x18000
	s_add_i32 s40, 0, 0x1c000
	v_add_u32_e32 v160, s39, v145
	v_add_u32_e32 v176, s40, v145
	ds_read_b128 v[148:151], v160
	ds_read_b128 v[152:155], v160 offset:1024
	ds_read_b128 v[156:159], v160 offset:2048
	ds_read_b128 v[160:163], v160 offset:3072
	ds_read_b128 v[164:167], v176
	ds_read_b128 v[168:171], v176 offset:1024
	ds_read_b128 v[172:175], v176 offset:2048
	ds_read_b128 v[176:179], v176 offset:3072
	s_add_u32 s22, s22, 0x80000
	s_addc_u32 s23, s23, 0
	s_mov_b32 m0, s29
	v_lshl_add_u64 v[224:225], s[22:23], 0, v[136:137]
	ds_read_b128 v[180:183], v147 offset:32768
	ds_read_b128 v[184:187], v147 offset:33792
	ds_read_b128 v[188:191], v147 offset:34816
	ds_read_b128 v[198:201], v147 offset:35840
	ds_read_b128 v[202:205], v147 offset:36864
	ds_read_b128 v[206:209], v147 offset:37888
	ds_read_b128 v[210:213], v147 offset:38912
	ds_read_b128 v[214:217], v147 offset:39936
	global_load_lds_dwordx4 v[224:225], off
	v_lshl_add_u64 v[224:225], s[22:23], 0, v[134:135]
	s_mov_b32 m0, s30
	s_nop 0
	global_load_lds_dwordx4 v[224:225], off
	s_waitcnt vmcnt(8)
	s_waitcnt lgkmcnt(0)
	s_barrier
	s_setprio 1
	s_waitcnt lgkmcnt(0)
	v_mfma_f32_16x16x32_bf16 v[126:129], v[148:151], v[180:183], v[126:129]
	v_mfma_f32_16x16x32_bf16 v[122:125], v[156:159], v[180:183], v[122:125]
	v_mfma_f32_16x16x32_bf16 v[110:113], v[148:151], v[188:191], v[110:113]
	v_mfma_f32_16x16x32_bf16 v[106:109], v[156:159], v[188:191], v[106:109]
	v_mfma_f32_16x16x32_bf16 v[94:97], v[148:151], v[202:205], v[94:97]
	v_mfma_f32_16x16x32_bf16 v[90:93], v[156:159], v[202:205], v[90:93]
	v_mfma_f32_16x16x32_bf16 v[78:81], v[148:151], v[210:213], v[78:81]
	v_mfma_f32_16x16x32_bf16 v[74:77], v[156:159], v[210:213], v[74:77]
	v_mfma_f32_16x16x32_bf16 v[126:129], v[152:155], v[184:187], v[126:129]
	v_mfma_f32_16x16x32_bf16 v[122:125], v[160:163], v[184:187], v[122:125]
	v_mfma_f32_16x16x32_bf16 v[110:113], v[152:155], v[198:201], v[110:113]
	v_mfma_f32_16x16x32_bf16 v[106:109], v[160:163], v[198:201], v[106:109]
	v_mfma_f32_16x16x32_bf16 v[94:97], v[152:155], v[206:209], v[94:97]
	v_mfma_f32_16x16x32_bf16 v[90:93], v[160:163], v[206:209], v[90:93]
	v_mfma_f32_16x16x32_bf16 v[78:81], v[152:155], v[214:217], v[78:81]
	v_mfma_f32_16x16x32_bf16 v[74:77], v[160:163], v[214:217], v[74:77]
	s_setprio 0
	s_setprio 1
	v_mfma_f32_16x16x32_bf16 v[118:121], v[164:167], v[180:183], v[118:121]
	v_mfma_f32_16x16x32_bf16 v[114:117], v[172:175], v[180:183], v[114:117]
	v_mfma_f32_16x16x32_bf16 v[102:105], v[164:167], v[188:191], v[102:105]
	v_mfma_f32_16x16x32_bf16 v[98:101], v[172:175], v[188:191], v[98:101]
	v_mfma_f32_16x16x32_bf16 v[86:89], v[164:167], v[202:205], v[86:89]
	v_mfma_f32_16x16x32_bf16 v[82:85], v[172:175], v[202:205], v[82:85]
	v_mfma_f32_16x16x32_bf16 v[70:73], v[164:167], v[210:213], v[70:73]
	v_mfma_f32_16x16x32_bf16 v[66:69], v[172:175], v[210:213], v[66:69]
	v_mfma_f32_16x16x32_bf16 v[118:121], v[168:171], v[184:187], v[118:121]
	v_mfma_f32_16x16x32_bf16 v[114:117], v[176:179], v[184:187], v[114:117]
	v_mfma_f32_16x16x32_bf16 v[102:105], v[168:171], v[198:201], v[102:105]
	v_mfma_f32_16x16x32_bf16 v[98:101], v[176:179], v[198:201], v[98:101]
	v_mfma_f32_16x16x32_bf16 v[86:89], v[168:171], v[206:209], v[86:89]
	v_mfma_f32_16x16x32_bf16 v[82:85], v[176:179], v[206:209], v[82:85]
	v_mfma_f32_16x16x32_bf16 v[70:73], v[168:171], v[214:217], v[70:73]
	v_mfma_f32_16x16x32_bf16 v[66:69], v[176:179], v[214:217], v[66:69]
	s_setprio 0
	s_barrier
	s_add_i32 s22, s39, s26
	v_lshl_add_u64 v[142:143], v[142:143], 0, s[84:85]
	s_mov_b32 m0, s22
	ds_read_b128 v[180:183], v147 offset:49152
	ds_read_b128 v[184:187], v147 offset:50176
	ds_read_b128 v[188:191], v147 offset:51200
	ds_read_b128 v[198:201], v147 offset:52224
	ds_read_b128 v[202:205], v147 offset:53248
	ds_read_b128 v[206:209], v147 offset:54272
	ds_read_b128 v[210:213], v147 offset:55296
	ds_read_b128 v[214:217], v147 offset:56320
	global_load_lds_dwordx4 v[142:143], off
	s_add_i32 m0, s22, 0x2000
	s_add_u32 s20, s20, 0x80080
	v_lshl_add_u64 v[142:143], v[218:219], 0, s[84:85]
	s_addc_u32 s21, s21, 0
	s_add_i32 s22, s40, s26
	global_load_lds_dwordx4 v[142:143], off
	v_lshl_add_u64 v[142:143], s[20:21], 0, v[130:131]
	s_mov_b32 m0, s22
	s_nop 0
	global_load_lds_dwordx4 v[142:143], off
	v_lshl_add_u64 v[142:143], s[20:21], 0, v[132:133]
	s_add_i32 m0, s22, 0x2000
	s_nop 0
	global_load_lds_dwordx4 v[142:143], off
	v_lshl_add_u64 v[142:143], v[220:221], 0, s[84:85]
	s_mov_b32 m0, s31
	s_nop 0
	global_load_lds_dwordx4 v[142:143], off
	v_lshl_add_u64 v[142:143], v[222:223], 0, s[84:85]
	s_mov_b32 m0, s34
	s_nop 0
	global_load_lds_dwordx4 v[142:143], off
	s_waitcnt vmcnt(8)
	s_waitcnt lgkmcnt(0)
	s_barrier
	s_setprio 1
	s_waitcnt lgkmcnt(0)
	v_mfma_f32_16x16x32_bf16 v[62:65], v[148:151], v[180:183], v[62:65]
	v_mfma_f32_16x16x32_bf16 v[58:61], v[156:159], v[180:183], v[58:61]
	v_mfma_f32_16x16x32_bf16 v[46:49], v[148:151], v[188:191], v[46:49]
	v_mfma_f32_16x16x32_bf16 v[42:45], v[156:159], v[188:191], v[42:45]
	v_mfma_f32_16x16x32_bf16 v[30:33], v[148:151], v[202:205], v[30:33]
	v_mfma_f32_16x16x32_bf16 v[26:29], v[156:159], v[202:205], v[26:29]
	v_mfma_f32_16x16x32_bf16 v[14:17], v[148:151], v[210:213], v[14:17]
	v_mfma_f32_16x16x32_bf16 v[10:13], v[156:159], v[210:213], v[10:13]
	v_mfma_f32_16x16x32_bf16 v[62:65], v[152:155], v[184:187], v[62:65]
	v_mfma_f32_16x16x32_bf16 v[58:61], v[160:163], v[184:187], v[58:61]
	v_mfma_f32_16x16x32_bf16 v[46:49], v[152:155], v[198:201], v[46:49]
	v_mfma_f32_16x16x32_bf16 v[42:45], v[160:163], v[198:201], v[42:45]
	v_mfma_f32_16x16x32_bf16 v[30:33], v[152:155], v[206:209], v[30:33]
	v_mfma_f32_16x16x32_bf16 v[26:29], v[160:163], v[206:209], v[26:29]
	v_mfma_f32_16x16x32_bf16 v[14:17], v[152:155], v[214:217], v[14:17]
	v_mfma_f32_16x16x32_bf16 v[10:13], v[160:163], v[214:217], v[10:13]
	s_setprio 0
	s_setprio 1
	v_mfma_f32_16x16x32_bf16 v[54:57], v[164:167], v[180:183], v[54:57]
	v_mfma_f32_16x16x32_bf16 v[50:53], v[172:175], v[180:183], v[50:53]
	v_mfma_f32_16x16x32_bf16 v[38:41], v[164:167], v[188:191], v[38:41]
	v_mfma_f32_16x16x32_bf16 v[34:37], v[172:175], v[188:191], v[34:37]
	v_mfma_f32_16x16x32_bf16 v[22:25], v[164:167], v[202:205], v[22:25]
	v_mfma_f32_16x16x32_bf16 v[18:21], v[172:175], v[202:205], v[18:21]
	v_mfma_f32_16x16x32_bf16 v[6:9], v[164:167], v[210:213], v[6:9]
	v_mfma_f32_16x16x32_bf16 v[2:5], v[172:175], v[210:213], v[2:5]
	v_mfma_f32_16x16x32_bf16 v[54:57], v[168:171], v[184:187], v[54:57]
	v_mfma_f32_16x16x32_bf16 v[50:53], v[176:179], v[184:187], v[50:53]
	v_mfma_f32_16x16x32_bf16 v[38:41], v[168:171], v[198:201], v[38:41]
	v_mfma_f32_16x16x32_bf16 v[34:37], v[176:179], v[198:201], v[34:37]
	v_mfma_f32_16x16x32_bf16 v[22:25], v[168:171], v[206:209], v[22:25]
	v_mfma_f32_16x16x32_bf16 v[18:21], v[176:179], v[206:209], v[18:21]
	v_mfma_f32_16x16x32_bf16 v[6:9], v[168:171], v[214:217], v[6:9]
	v_mfma_f32_16x16x32_bf16 v[2:5], v[176:179], v[214:217], v[2:5]
	s_setprio 0
	s_barrier
	s_add_i32 s38, s38, 2
	s_add_u32 s18, s18, 0x100
	s_addc_u32 s19, s19, 0
	s_add_u32 s9, s9, 0x100
	s_addc_u32 s11, s11, 0
	s_cmp_gt_u32 s38, 29
	s_cbranch_scc0 .LBB0_1397
